# hybrid K1 ring 24 (24KiB chunks, 10 private + queues) + last-chunk early flush
# baseline (speedup 1.0000x reference)
.Lk1_scan:
	s_load_dwordx2 s[4:5], s[0:1], 0x0
	s_load_dwordx4 s[8:11], s[0:1], 0x20
	s_load_dwordx2 s[12:13], s[0:1], 0x30
	v_and_b32_e32 v6, 63, v0
	v_readfirstlane_b32 s3, v0
	v_lshlrev_b32_e32 v1, 4, v6
	v_lshlrev_b32_e32 v2, 2, v6
	v_or_b32_e32 v3, 1, v2
	v_or_b32_e32 v4, 2, v2
	v_or_b32_e32 v5, 3, v2
	s_lshr_b32 s3, s3, 6
	s_sub_u32 s16, s2, 0x60
	s_lshl_b32 s16, s16, 2
	s_add_u32 s16, s16, s3
	s_mul_i32 s17, s16, 0x48000
	s_lshr_b32 s18, s17, 2
	s_lshl_b32 s24, s3, 13
	s_mov_b32 s25, s24
	s_mov_b32 s28, s24
	s_mov_b32 s36, 0
	s_mov_b64 s[62:63], 0
	v_mov_b32_e32 v21, 1
	s_mov_b32 s27, 0
	s_mov_b32 s29, 0x55555556
	s_mov_b32 s31, 0xc0000
	s_waitcnt lgkmcnt(0)
	s_and_b32 s50, s16, 15
	s_mul_i32 s52, s50, 256
	s_add_u32 s52, s52, 20480
	s_lshl_b32 s53, s50, 6
	s_add_u32 s53, s53, 0xe000
	s_add_u32 s54, s10, s53
	s_addc_u32 s55, s11, 0
	s_mul_i32 s59, s16, 10
	s_mul_i32 s57, s59, 0x6000
	s_lshr_b32 s18, s57, 2
	s_add_u32 s6, s4, s57
	s_addc_u32 s7, s5, 0
	v_mov_b32_e32 v27, 0
	global_load_dwordx4 v[28:31], v1, s[6:7] nt
	s_add_u32 s6, s6, 0x400
	s_addc_u32 s7, s7, 0
	global_load_dwordx4 v[32:35], v1, s[6:7] nt
	s_add_u32 s6, s6, 0x400
	s_addc_u32 s7, s7, 0
	global_load_dwordx4 v[36:39], v1, s[6:7] nt
	s_add_u32 s6, s6, 0x400
	s_addc_u32 s7, s7, 0
	global_load_dwordx4 v[40:43], v1, s[6:7] nt
	s_add_u32 s6, s6, 0x400
	s_addc_u32 s7, s7, 0
	global_load_dwordx4 v[44:47], v1, s[6:7] nt
	s_add_u32 s6, s6, 0x400
	s_addc_u32 s7, s7, 0
	global_load_dwordx4 v[48:51], v1, s[6:7] nt
	s_add_u32 s6, s6, 0x400
	s_addc_u32 s7, s7, 0
	global_load_dwordx4 v[52:55], v1, s[6:7] nt
	s_add_u32 s6, s6, 0x400
	s_addc_u32 s7, s7, 0
	global_load_dwordx4 v[56:59], v1, s[6:7] nt
	s_add_u32 s6, s6, 0x400
	s_addc_u32 s7, s7, 0
	global_load_dwordx4 v[60:63], v1, s[6:7] nt
	s_add_u32 s6, s6, 0x400
	s_addc_u32 s7, s7, 0
	global_load_dwordx4 v[64:67], v1, s[6:7] nt
	s_add_u32 s6, s6, 0x400
	s_addc_u32 s7, s7, 0
	global_load_dwordx4 v[68:71], v1, s[6:7] nt
	s_add_u32 s6, s6, 0x400
	s_addc_u32 s7, s7, 0
	global_load_dwordx4 v[72:75], v1, s[6:7] nt
	s_add_u32 s6, s6, 0x400
	s_addc_u32 s7, s7, 0
	global_load_dwordx4 v[76:79], v1, s[6:7] nt
	s_add_u32 s6, s6, 0x400
	s_addc_u32 s7, s7, 0
	global_load_dwordx4 v[80:83], v1, s[6:7] nt
	s_add_u32 s6, s6, 0x400
	s_addc_u32 s7, s7, 0
	global_load_dwordx4 v[84:87], v1, s[6:7] nt
	s_add_u32 s6, s6, 0x400
	s_addc_u32 s7, s7, 0
	global_load_dwordx4 v[88:91], v1, s[6:7] nt
	s_add_u32 s6, s6, 0x400
	s_addc_u32 s7, s7, 0
	global_load_dwordx4 v[92:95], v1, s[6:7] nt
	s_add_u32 s6, s6, 0x400
	s_addc_u32 s7, s7, 0
	global_load_dwordx4 v[96:99], v1, s[6:7] nt
	s_add_u32 s6, s6, 0x400
	s_addc_u32 s7, s7, 0
	global_load_dwordx4 v[100:103], v1, s[6:7] nt
	s_add_u32 s6, s6, 0x400
	s_addc_u32 s7, s7, 0
	global_load_dwordx4 v[104:107], v1, s[6:7] nt
	s_add_u32 s6, s6, 0x400
	s_addc_u32 s7, s7, 0
	global_load_dwordx4 v[108:111], v1, s[6:7] nt
	s_add_u32 s6, s6, 0x400
	s_addc_u32 s7, s7, 0
	global_load_dwordx4 v[112:115], v1, s[6:7] nt
	s_add_u32 s6, s6, 0x400
	s_addc_u32 s7, s7, 0
	global_load_dwordx4 v[116:119], v1, s[6:7] nt
	s_add_u32 s6, s6, 0x400
	s_addc_u32 s7, s7, 0
	global_load_dwordx4 v[120:123], v1, s[6:7] nt
	s_add_u32 s6, s6, 0x400
	s_addc_u32 s7, s7, 0
	s_mov_b32 s26, 12
	s_add_u32 s57, s59, 1
	s_mul_i32 s57, s57, 0x6000
	s_lshr_b32 s58, s57, 2
	s_add_u32 s6, s4, s57
	s_addc_u32 s7, s5, 0
	s_mov_b32 s26, 0
.Lk1_main:
	s_waitcnt vmcnt(23)
	v_or3_b32 v12, v28, v29, v30
	v_or_b32_e32 v12, v12, v31
	v_cmp_ne_u32_e32 vcc, 0, v12
	s_cbranch_vccnz .Lk1_hitm_0
.Lk1_contm_0:
	s_waitcnt vmcnt(22)
	v_or3_b32 v12, v32, v33, v34
	v_or_b32_e32 v12, v12, v35
	v_cmp_ne_u32_e32 vcc, 0, v12
	s_cbranch_vccnz .Lk1_hitm_1
.Lk1_contm_1:
	s_waitcnt vmcnt(21)
	v_or3_b32 v12, v36, v37, v38
	v_or_b32_e32 v12, v12, v39
	v_cmp_ne_u32_e32 vcc, 0, v12
	s_cbranch_vccnz .Lk1_hitm_2
.Lk1_contm_2:
	s_waitcnt vmcnt(20)
	v_or3_b32 v12, v40, v41, v42
	v_or_b32_e32 v12, v12, v43
	v_cmp_ne_u32_e32 vcc, 0, v12
	s_cbranch_vccnz .Lk1_hitm_3
.Lk1_contm_3:
	s_waitcnt vmcnt(19)
	v_or3_b32 v12, v44, v45, v46
	v_or_b32_e32 v12, v12, v47
	v_cmp_ne_u32_e32 vcc, 0, v12
	s_cbranch_vccnz .Lk1_hitm_4
.Lk1_contm_4:
	s_waitcnt vmcnt(18)
	v_or3_b32 v12, v48, v49, v50
	v_or_b32_e32 v12, v12, v51
	v_cmp_ne_u32_e32 vcc, 0, v12
	s_cbranch_vccnz .Lk1_hitm_5
.Lk1_contm_5:
	s_waitcnt vmcnt(17)
	v_or3_b32 v12, v52, v53, v54
	v_or_b32_e32 v12, v12, v55
	v_cmp_ne_u32_e32 vcc, 0, v12
	s_cbranch_vccnz .Lk1_hitm_6
.Lk1_contm_6:
	s_waitcnt vmcnt(16)
	v_or3_b32 v12, v56, v57, v58
	v_or_b32_e32 v12, v12, v59
	v_cmp_ne_u32_e32 vcc, 0, v12
	s_cbranch_vccnz .Lk1_hitm_7
.Lk1_contm_7:
	global_load_dwordx4 v[28:31], v1, s[6:7] nt
	s_add_u32 s6, s6, 0x400
	s_addc_u32 s7, s7, 0
	global_load_dwordx4 v[32:35], v1, s[6:7] nt
	s_add_u32 s6, s6, 0x400
	s_addc_u32 s7, s7, 0
	global_load_dwordx4 v[36:39], v1, s[6:7] nt
	s_add_u32 s6, s6, 0x400
	s_addc_u32 s7, s7, 0
	global_load_dwordx4 v[40:43], v1, s[6:7] nt
	s_add_u32 s6, s6, 0x400
	s_addc_u32 s7, s7, 0
	global_load_dwordx4 v[44:47], v1, s[6:7] nt
	s_add_u32 s6, s6, 0x400
	s_addc_u32 s7, s7, 0
	global_load_dwordx4 v[48:51], v1, s[6:7] nt
	s_add_u32 s6, s6, 0x400
	s_addc_u32 s7, s7, 0
	global_load_dwordx4 v[52:55], v1, s[6:7] nt
	s_add_u32 s6, s6, 0x400
	s_addc_u32 s7, s7, 0
	global_load_dwordx4 v[56:59], v1, s[6:7] nt
	s_add_u32 s6, s6, 0x400
	s_addc_u32 s7, s7, 0
	s_waitcnt vmcnt(23)
	v_or3_b32 v12, v60, v61, v62
	v_or_b32_e32 v12, v12, v63
	v_cmp_ne_u32_e32 vcc, 0, v12
	s_cbranch_vccnz .Lk1_hitm_8

.Lk1_contm_15:
	global_load_dwordx4 v[60:63], v1, s[6:7] nt
	s_add_u32 s6, s6, 0x400
	s_addc_u32 s7, s7, 0
	global_load_dwordx4 v[64:67], v1, s[6:7] nt
	s_add_u32 s6, s6, 0x400
	s_addc_u32 s7, s7, 0
	global_load_dwordx4 v[68:71], v1, s[6:7] nt
	s_add_u32 s6, s6, 0x400
	s_addc_u32 s7, s7, 0
	global_load_dwordx4 v[72:75], v1, s[6:7] nt
	s_add_u32 s6, s6, 0x400
	s_addc_u32 s7, s7, 0
	global_load_dwordx4 v[76:79], v1, s[6:7] nt
	s_add_u32 s6, s6, 0x400
	s_addc_u32 s7, s7, 0
	global_load_dwordx4 v[80:83], v1, s[6:7] nt
	s_add_u32 s6, s6, 0x400
	s_addc_u32 s7, s7, 0
	global_load_dwordx4 v[84:87], v1, s[6:7] nt
	s_add_u32 s6, s6, 0x400
	s_addc_u32 s7, s7, 0
	global_load_dwordx4 v[88:91], v1, s[6:7] nt
	s_add_u32 s6, s6, 0x400
	s_addc_u32 s7, s7, 0
	s_waitcnt vmcnt(23)
	v_or3_b32 v12, v92, v93, v94
	v_or_b32_e32 v12, v12, v95
	v_cmp_ne_u32_e32 vcc, 0, v12
	s_cbranch_vccnz .Lk1_hitm_16
.Lk1_contm_16:
	s_waitcnt vmcnt(22)
	v_or3_b32 v12, v96, v97, v98
	v_or_b32_e32 v12, v12, v99
	v_cmp_ne_u32_e32 vcc, 0, v12
	s_cbranch_vccnz .Lk1_hitm_17
.Lk1_contm_17:
	s_waitcnt vmcnt(21)
	v_or3_b32 v12, v100, v101, v102
	v_or_b32_e32 v12, v12, v103
	v_cmp_ne_u32_e32 vcc, 0, v12
	s_cbranch_vccnz .Lk1_hitm_18
.Lk1_contm_18:
	s_waitcnt vmcnt(20)
	v_or3_b32 v12, v104, v105, v106
	v_or_b32_e32 v12, v12, v107
	v_cmp_ne_u32_e32 vcc, 0, v12
	s_cbranch_vccnz .Lk1_hitm_19
.Lk1_contm_19:
	s_waitcnt vmcnt(19)
	v_or3_b32 v12, v108, v109, v110
	v_or_b32_e32 v12, v12, v111
	v_cmp_ne_u32_e32 vcc, 0, v12
	s_cbranch_vccnz .Lk1_hitm_20
.Lk1_contm_20:
	s_waitcnt vmcnt(18)
	v_or3_b32 v12, v112, v113, v114
	v_or_b32_e32 v12, v12, v115
	v_cmp_ne_u32_e32 vcc, 0, v12
	s_cbranch_vccnz .Lk1_hitm_21
.Lk1_contm_21:
	s_waitcnt vmcnt(17)
	v_or3_b32 v12, v116, v117, v118
	v_or_b32_e32 v12, v12, v119
	v_cmp_ne_u32_e32 vcc, 0, v12
	s_cbranch_vccnz .Lk1_hitm_22
.Lk1_contm_22:
	s_waitcnt vmcnt(16)
	v_or3_b32 v12, v120, v121, v122
	v_or_b32_e32 v12, v12, v123
	v_cmp_ne_u32_e32 vcc, 0, v12
	s_cbranch_vccnz .Lk1_hitm_23
.Lk1_contm_23:
	global_load_dwordx4 v[92:95], v1, s[6:7] nt
	s_add_u32 s6, s6, 0x400
	s_addc_u32 s7, s7, 0
	global_load_dwordx4 v[96:99], v1, s[6:7] nt
	s_add_u32 s6, s6, 0x400
	s_addc_u32 s7, s7, 0
	global_load_dwordx4 v[100:103], v1, s[6:7] nt
	s_add_u32 s6, s6, 0x400
	s_addc_u32 s7, s7, 0
	global_load_dwordx4 v[104:107], v1, s[6:7] nt
	s_add_u32 s6, s6, 0x400
	s_addc_u32 s7, s7, 0
	global_load_dwordx4 v[108:111], v1, s[6:7] nt
	s_add_u32 s6, s6, 0x400
	s_addc_u32 s7, s7, 0
	global_load_dwordx4 v[112:115], v1, s[6:7] nt
	s_add_u32 s6, s6, 0x400
	s_addc_u32 s7, s7, 0
	global_load_dwordx4 v[116:119], v1, s[6:7] nt
	s_add_u32 s6, s6, 0x400
	s_addc_u32 s7, s7, 0
	global_load_dwordx4 v[120:123], v1, s[6:7] nt
	s_add_u32 s6, s6, 0x400
	s_addc_u32 s7, s7, 0
	s_mov_b32 s18, s58
	s_add_u32 s60, s26, 2
	s_cmp_lt_u32 s60, 10
	s_cbranch_scc0 .Lk1_dynid
	s_add_u32 s57, s59, s60
	s_branch .Lk1_haveid

.Lk1_haveid:
	s_mul_i32 s57, s57, 0x6000
	s_lshr_b32 s58, s57, 2
	s_add_u32 s6, s4, s57
	s_addc_u32 s7, s5, 0
	s_add_u32 s60, s26, 3
	s_cmp_lt_u32 s60, 10
	s_cbranch_scc1 .Lk1_noreq
	s_mov_b64 exec, 1
	global_atomic_add v26, v27, v21, s[54:55] sc0
	s_mov_b64 exec, -1

.Lk1_inone_l:
	s_cmp_ge_u32 s28, s25
	s_cbranch_scc1 .Lk1_inone_lx
	s_waitcnt lgkmcnt(0)
	v_lshl_add_u32 v25, v6, 3, s28
	v_cmp_gt_u32_e32 vcc, s25, v25
	s_and_saveexec_b64 s[32:33], vcc
	s_mov_b64 s[62:63], exec
	ds_read_b64 v[124:125], v25
	s_waitcnt lgkmcnt(0)
	v_lshrrev_b32_e32 v129, 12, v124
	v_mul_hi_u32 v129, v129, s29
	v_mul_u32_u24_e32 v126, 0x3000, v129
	v_sub_u32_e32 v126, v124, v126
	v_lshlrev_b32_e32 v127, 2, v126
	global_atomic_add v128, v127, v21, s[8:9] sc0
	global_atomic_add_f32 v127, v125, s[10:11]
	v_mov_b32_e32 v124, v129
	s_mov_b64 exec, -1
	s_add_u32 s28, s28, 0x200
	s_cmp_ge_u32 s28, s25
	s_cbranch_scc0 .Lk1_inone_lx
	s_mov_b32 s28, s24
	s_mov_b32 s25, s24

.Lk1_contl_7:
	s_waitcnt vmcnt(15)
	v_or3_b32 v12, v60, v61, v62
	v_or_b32_e32 v12, v12, v63
	v_cmp_ne_u32_e32 vcc, 0, v12
	s_cbranch_vccnz .Lk1_hitl_8

.Lk1_contl_15:
	s_waitcnt vmcnt(7)
	v_or3_b32 v12, v92, v93, v94
	v_or_b32_e32 v12, v12, v95
	v_cmp_ne_u32_e32 vcc, 0, v12
	s_cbranch_vccnz .Lk1_hitl_16
.Lk1_contl_16:
	s_waitcnt vmcnt(6)
	v_or3_b32 v12, v96, v97, v98
	v_or_b32_e32 v12, v12, v99
	v_cmp_ne_u32_e32 vcc, 0, v12
	s_cbranch_vccnz .Lk1_hitl_17
.Lk1_contl_17:
	s_waitcnt vmcnt(5)
	v_or3_b32 v12, v100, v101, v102
	v_or_b32_e32 v12, v12, v103
	v_cmp_ne_u32_e32 vcc, 0, v12
	s_cbranch_vccnz .Lk1_hitl_18
.Lk1_contl_18:
	s_waitcnt vmcnt(4)
	v_or3_b32 v12, v104, v105, v106
	v_or_b32_e32 v12, v12, v107
	v_cmp_ne_u32_e32 vcc, 0, v12
	s_cbranch_vccnz .Lk1_hitl_19
.Lk1_contl_19:
	s_waitcnt vmcnt(3)
	v_or3_b32 v12, v108, v109, v110
	v_or_b32_e32 v12, v12, v111
	v_cmp_ne_u32_e32 vcc, 0, v12
	s_cbranch_vccnz .Lk1_hitl_20
.Lk1_contl_20:
	s_waitcnt vmcnt(2)
	v_or3_b32 v12, v112, v113, v114
	v_or_b32_e32 v12, v12, v115
	v_cmp_ne_u32_e32 vcc, 0, v12
	s_cbranch_vccnz .Lk1_hitl_21
.Lk1_contl_21:
	s_waitcnt vmcnt(1)
	v_or3_b32 v12, v116, v117, v118
	v_or_b32_e32 v12, v12, v119
	v_cmp_ne_u32_e32 vcc, 0, v12
	s_cbranch_vccnz .Lk1_hitl_22
.Lk1_contl_22:
	s_waitcnt vmcnt(0)
	v_or3_b32 v12, v120, v121, v122
	v_or_b32_e32 v12, v12, v123
	v_cmp_ne_u32_e32 vcc, 0, v12
	s_cbranch_vccnz .Lk1_hitl_23

.Lk1_cskip_fin_pend:
	s_mov_b64 exec, s[62:63]
	s_cbranch_execz .Lk1_cskip_fin_x
	v_mul_u32_u24_e32 v130, 0x3000, v126
	v_lshlrev_b32_e32 v129, 6, v126
	v_cmp_gt_u32_e32 vcc, 64, v128
	v_add_u32_e32 v129, v129, v128
	v_add3_u32 v130, v130, v128, s31
	v_cndmask_b32_e32 v129, v130, v129, vcc
	v_lshlrev_b32_e32 v129, 3, v129
	global_store_dwordx2 v129, v[124:125], s[12:13]

.Lk1_hitl_0:
	v_mov_b32_e32 v8, v28
	v_mov_b32_e32 v9, v29
	v_mov_b32_e32 v10, v30
	v_mov_b32_e32 v11, v31
	s_mov_b32 s19, s18
	s_movk_i32 s23, 24
	s_branch .Lk1_slow
.Lk1_hitl_1:
	v_mov_b32_e32 v8, v32
	v_mov_b32_e32 v9, v33
	v_mov_b32_e32 v10, v34
	v_mov_b32_e32 v11, v35
	s_add_u32 s19, s18, 0x100
	s_movk_i32 s23, 25
	s_branch .Lk1_slow
.Lk1_hitl_2:
	v_mov_b32_e32 v8, v36
	v_mov_b32_e32 v9, v37
	v_mov_b32_e32 v10, v38
	v_mov_b32_e32 v11, v39
	s_add_u32 s19, s18, 0x200
	s_movk_i32 s23, 26
	s_branch .Lk1_slow
.Lk1_hitl_3:
	v_mov_b32_e32 v8, v40
	v_mov_b32_e32 v9, v41
	v_mov_b32_e32 v10, v42
	v_mov_b32_e32 v11, v43
	s_add_u32 s19, s18, 0x300
	s_movk_i32 s23, 27
	s_branch .Lk1_slow
.Lk1_hitl_4:
	v_mov_b32_e32 v8, v44
	v_mov_b32_e32 v9, v45
	v_mov_b32_e32 v10, v46
	v_mov_b32_e32 v11, v47
	s_add_u32 s19, s18, 0x400
	s_movk_i32 s23, 28
	s_branch .Lk1_slow
.Lk1_hitl_5:
	v_mov_b32_e32 v8, v48
	v_mov_b32_e32 v9, v49
	v_mov_b32_e32 v10, v50
	v_mov_b32_e32 v11, v51
	s_add_u32 s19, s18, 0x500
	s_movk_i32 s23, 29
	s_branch .Lk1_slow
.Lk1_hitl_6:
	v_mov_b32_e32 v8, v52
	v_mov_b32_e32 v9, v53
	v_mov_b32_e32 v10, v54
	v_mov_b32_e32 v11, v55
	s_add_u32 s19, s18, 0x600
	s_movk_i32 s23, 30
	s_branch .Lk1_slow
.Lk1_hitl_7:
	v_mov_b32_e32 v8, v56
	v_mov_b32_e32 v9, v57
	v_mov_b32_e32 v10, v58
	v_mov_b32_e32 v11, v59
	s_add_u32 s19, s18, 0x700
	s_movk_i32 s23, 31
	s_branch .Lk1_slow
.Lk1_hitl_8:
	v_mov_b32_e32 v8, v60
	v_mov_b32_e32 v9, v61
	v_mov_b32_e32 v10, v62
	v_mov_b32_e32 v11, v63
	s_add_u32 s19, s18, 0x800
	s_movk_i32 s23, 32
	s_branch .Lk1_slow
.Lk1_hitl_9:
	v_mov_b32_e32 v8, v64
	v_mov_b32_e32 v9, v65
	v_mov_b32_e32 v10, v66
	v_mov_b32_e32 v11, v67
	s_add_u32 s19, s18, 0x900
	s_movk_i32 s23, 33
	s_branch .Lk1_slow
.Lk1_hitl_10:
	v_mov_b32_e32 v8, v68
	v_mov_b32_e32 v9, v69
	v_mov_b32_e32 v10, v70
	v_mov_b32_e32 v11, v71
	s_add_u32 s19, s18, 0xa00
	s_movk_i32 s23, 34
	s_branch .Lk1_slow
.Lk1_hitl_11:
	v_mov_b32_e32 v8, v72
	v_mov_b32_e32 v9, v73
	v_mov_b32_e32 v10, v74
	v_mov_b32_e32 v11, v75
	s_add_u32 s19, s18, 0xb00
	s_movk_i32 s23, 35
	s_branch .Lk1_slow
.Lk1_hitl_12:
	v_mov_b32_e32 v8, v76
	v_mov_b32_e32 v9, v77
	v_mov_b32_e32 v10, v78
	v_mov_b32_e32 v11, v79
	s_add_u32 s19, s18, 0xc00
	s_movk_i32 s23, 36
	s_branch .Lk1_slow
.Lk1_hitl_13:
	v_mov_b32_e32 v8, v80
	v_mov_b32_e32 v9, v81
	v_mov_b32_e32 v10, v82
	v_mov_b32_e32 v11, v83
	s_add_u32 s19, s18, 0xd00
	s_movk_i32 s23, 37
	s_branch .Lk1_slow
.Lk1_hitl_14:
	v_mov_b32_e32 v8, v84
	v_mov_b32_e32 v9, v85
	v_mov_b32_e32 v10, v86
	v_mov_b32_e32 v11, v87
	s_add_u32 s19, s18, 0xe00
	s_movk_i32 s23, 38
	s_branch .Lk1_slow
.Lk1_hitl_15:
	v_mov_b32_e32 v8, v88
	v_mov_b32_e32 v9, v89
	v_mov_b32_e32 v10, v90
	v_mov_b32_e32 v11, v91
	s_add_u32 s19, s18, 0xf00
	s_movk_i32 s23, 39
	s_branch .Lk1_slow
.Lk1_hitl_16:
	v_mov_b32_e32 v8, v92
	v_mov_b32_e32 v9, v93
	v_mov_b32_e32 v10, v94
	v_mov_b32_e32 v11, v95
	s_add_u32 s19, s18, 0x1000
	s_movk_i32 s23, 40
	s_branch .Lk1_slow
.Lk1_hitl_17:
	v_mov_b32_e32 v8, v96
	v_mov_b32_e32 v9, v97
	v_mov_b32_e32 v10, v98
	v_mov_b32_e32 v11, v99
	s_add_u32 s19, s18, 0x1100
	s_movk_i32 s23, 41
	s_branch .Lk1_slow
.Lk1_hitl_18:
	v_mov_b32_e32 v8, v100
	v_mov_b32_e32 v9, v101
	v_mov_b32_e32 v10, v102
	v_mov_b32_e32 v11, v103
	s_add_u32 s19, s18, 0x1200
	s_movk_i32 s23, 42
	s_branch .Lk1_slow
.Lk1_hitl_19:
	v_mov_b32_e32 v8, v104
	v_mov_b32_e32 v9, v105
	v_mov_b32_e32 v10, v106
	v_mov_b32_e32 v11, v107
	s_add_u32 s19, s18, 0x1300
	s_movk_i32 s23, 43
	s_branch .Lk1_slow
.Lk1_hitl_20:
	v_mov_b32_e32 v8, v108
	v_mov_b32_e32 v9, v109
	v_mov_b32_e32 v10, v110
	v_mov_b32_e32 v11, v111
	s_add_u32 s19, s18, 0x1400
	s_movk_i32 s23, 44
	s_branch .Lk1_slow
.Lk1_hitl_21:
	v_mov_b32_e32 v8, v112
	v_mov_b32_e32 v9, v113
	v_mov_b32_e32 v10, v114
	v_mov_b32_e32 v11, v115
	s_add_u32 s19, s18, 0x1500
	s_movk_i32 s23, 45
	s_branch .Lk1_slow
.Lk1_hitl_22:
	v_mov_b32_e32 v8, v116
	v_mov_b32_e32 v9, v117
	v_mov_b32_e32 v10, v118
	v_mov_b32_e32 v11, v119
	s_add_u32 s19, s18, 0x1600
	s_movk_i32 s23, 46
	s_branch .Lk1_slow
.Lk1_hitl_23:
	v_mov_b32_e32 v8, v120
	v_mov_b32_e32 v9, v121
	v_mov_b32_e32 v10, v122
	v_mov_b32_e32 v11, v123
	s_add_u32 s19, s18, 0x1700
	s_movk_i32 s23, 47
	s_branch .Lk1_slow

.Lk1_disp:
	s_cmp_lt_u32 s23, 24
	s_cbranch_scc1 .Lk1_d1
	s_cmp_lt_u32 s23, 36
	s_cbranch_scc1 .Lk1_d2
	s_cmp_lt_u32 s23, 42
	s_cbranch_scc1 .Lk1_d3
	s_cmp_lt_u32 s23, 45
	s_cbranch_scc1 .Lk1_d4
	s_cmp_lt_u32 s23, 46
	s_cbranch_scc1 .Lk1_d5
	s_cmp_lt_u32 s23, 47
	s_cbranch_scc1 .Lk1_d6
	s_branch .Lk1_contl_23
.Lk1_d6:
	s_branch .Lk1_contl_22
.Lk1_d5:
	s_branch .Lk1_contl_21
.Lk1_d4:
	s_cmp_lt_u32 s23, 43
	s_cbranch_scc1 .Lk1_d7
	s_cmp_lt_u32 s23, 44
	s_cbranch_scc1 .Lk1_d8
	s_branch .Lk1_contl_20
.Lk1_d8:
	s_branch .Lk1_contl_19
.Lk1_d7:
	s_branch .Lk1_contl_18
.Lk1_d3:
	s_cmp_lt_u32 s23, 39
	s_cbranch_scc1 .Lk1_d9
	s_cmp_lt_u32 s23, 40
	s_cbranch_scc1 .Lk1_d10
	s_cmp_lt_u32 s23, 41
	s_cbranch_scc1 .Lk1_d11
	s_branch .Lk1_contl_17
.Lk1_d11:
	s_branch .Lk1_contl_16
.Lk1_d10:
	s_branch .Lk1_contl_15
.Lk1_d9:
	s_cmp_lt_u32 s23, 37
	s_cbranch_scc1 .Lk1_d12
	s_cmp_lt_u32 s23, 38
	s_cbranch_scc1 .Lk1_d13
	s_branch .Lk1_contl_14
.Lk1_d13:
	s_branch .Lk1_contl_13
.Lk1_d12:
	s_branch .Lk1_contl_12
.Lk1_d2:
	s_cmp_lt_u32 s23, 30
	s_cbranch_scc1 .Lk1_d14
	s_cmp_lt_u32 s23, 33
	s_cbranch_scc1 .Lk1_d15
	s_cmp_lt_u32 s23, 34
	s_cbranch_scc1 .Lk1_d16
	s_cmp_lt_u32 s23, 35
	s_cbranch_scc1 .Lk1_d17
	s_branch .Lk1_contl_11
.Lk1_d17:
	s_branch .Lk1_contl_10
.Lk1_d16:
	s_branch .Lk1_contl_9
.Lk1_d15:
	s_cmp_lt_u32 s23, 31
	s_cbranch_scc1 .Lk1_d18
	s_cmp_lt_u32 s23, 32
	s_cbranch_scc1 .Lk1_d19
	s_branch .Lk1_contl_8
.Lk1_d19:
	s_branch .Lk1_contl_7
.Lk1_d18:
	s_branch .Lk1_contl_6
.Lk1_d14:
	s_cmp_lt_u32 s23, 27
	s_cbranch_scc1 .Lk1_d20
	s_cmp_lt_u32 s23, 28
	s_cbranch_scc1 .Lk1_d21
	s_cmp_lt_u32 s23, 29
	s_cbranch_scc1 .Lk1_d22
	s_branch .Lk1_contl_5
.Lk1_d22:
	s_branch .Lk1_contl_4
.Lk1_d21:
	s_branch .Lk1_contl_3
.Lk1_d20:
	s_cmp_lt_u32 s23, 25
	s_cbranch_scc1 .Lk1_d23
	s_cmp_lt_u32 s23, 26
	s_cbranch_scc1 .Lk1_d24
	s_branch .Lk1_contl_2
.Lk1_d24:
	s_branch .Lk1_contl_1
.Lk1_d23:
	s_branch .Lk1_contl_0
.Lk1_d1:
	s_cmp_lt_u32 s23, 12
	s_cbranch_scc1 .Lk1_d25
	s_cmp_lt_u32 s23, 18
	s_cbranch_scc1 .Lk1_d26
	s_cmp_lt_u32 s23, 21
	s_cbranch_scc1 .Lk1_d27
	s_cmp_lt_u32 s23, 22
	s_cbranch_scc1 .Lk1_d28
	s_cmp_lt_u32 s23, 23
	s_cbranch_scc1 .Lk1_d29
	s_branch .Lk1_contm_23
.Lk1_d29:
	s_branch .Lk1_contm_22
.Lk1_d28:
	s_branch .Lk1_contm_21
.Lk1_d27:
	s_cmp_lt_u32 s23, 19
	s_cbranch_scc1 .Lk1_d30
	s_cmp_lt_u32 s23, 20
	s_cbranch_scc1 .Lk1_d31
	s_branch .Lk1_contm_20
.Lk1_d31:
	s_branch .Lk1_contm_19
.Lk1_d30:
	s_branch .Lk1_contm_18
.Lk1_d26:
	s_cmp_lt_u32 s23, 15
	s_cbranch_scc1 .Lk1_d32
	s_cmp_lt_u32 s23, 16
	s_cbranch_scc1 .Lk1_d33
	s_cmp_lt_u32 s23, 17
	s_cbranch_scc1 .Lk1_d34
	s_branch .Lk1_contm_17
.Lk1_d34:
	s_branch .Lk1_contm_16
.Lk1_d33:
	s_branch .Lk1_contm_15
.Lk1_d32:
	s_cmp_lt_u32 s23, 13
	s_cbranch_scc1 .Lk1_d35
	s_cmp_lt_u32 s23, 14
	s_cbranch_scc1 .Lk1_d36
	s_branch .Lk1_contm_14
.Lk1_d36:
	s_branch .Lk1_contm_13
.Lk1_d35:
	s_branch .Lk1_contm_12
.Lk1_d25:
	s_cmp_lt_u32 s23, 6
	s_cbranch_scc1 .Lk1_d37
	s_cmp_lt_u32 s23, 9
	s_cbranch_scc1 .Lk1_d38
	s_cmp_lt_u32 s23, 10
	s_cbranch_scc1 .Lk1_d39
	s_cmp_lt_u32 s23, 11
	s_cbranch_scc1 .Lk1_d40
	s_branch .Lk1_contm_11
.Lk1_d40:
	s_branch .Lk1_contm_10
.Lk1_d39:
	s_branch .Lk1_contm_9
.Lk1_d38:
	s_cmp_lt_u32 s23, 7
	s_cbranch_scc1 .Lk1_d41
	s_cmp_lt_u32 s23, 8
	s_cbranch_scc1 .Lk1_d42
	s_branch .Lk1_contm_8
.Lk1_d42:
	s_branch .Lk1_contm_7
.Lk1_d41:
	s_branch .Lk1_contm_6
.Lk1_d37:
	s_cmp_lt_u32 s23, 3
	s_cbranch_scc1 .Lk1_d43
	s_cmp_lt_u32 s23, 4
	s_cbranch_scc1 .Lk1_d44
	s_cmp_lt_u32 s23, 5
	s_cbranch_scc1 .Lk1_d45
	s_branch .Lk1_contm_5
.Lk1_d45:
	s_branch .Lk1_contm_4
.Lk1_d44:
	s_branch .Lk1_contm_3
.Lk1_d43:
	s_cmp_lt_u32 s23, 1
	s_cbranch_scc1 .Lk1_d46
	s_cmp_lt_u32 s23, 2
	s_cbranch_scc1 .Lk1_d47
	s_branch .Lk1_contm_2
.Lk1_d47:
	s_branch .Lk1_contm_1
.Lk1_d46:
	s_branch .Lk1_contm_0
